# P8: workgroups without a router unit convert 5 of each WG's expert-weight items there (was idle time); P2 split kept
# speedup vs baseline: 1.0358x; 1.0136x over previous
.LBB0_174:
	s_lshl_b32 s22, s36, 20
	s_lshl_b32 s23, s36, 28
	s_waitcnt vmcnt(3)
	v_mov_b32_e32 v2, v0
	s_mov_b64 s[0:1], s[42:43]
	s_add_u32 s19, s0, 0x10a4c000
	s_addc_u32 s20, s1, 0
	s_add_u32 s2, s0, 0x14a4c000
	s_addc_u32 s3, s1, 0
	s_add_u32 s4, s0, 0x894c000
	s_addc_u32 s5, s1, 0
	v_readfirstlane_b32 s10, v2
	s_add_u32 s21, s0, 0x94c000
	s_addc_u32 s24, s1, 0
	v_lshlrev_b32_e32 v3, 1, v2
	s_ashr_i32 s0, s10, 1
	v_and_b32_e32 v70, 0x70, v3
	s_and_b32 s10, s0, 0xffffffe0
	v_lshlrev_b32_e32 v3, 2, v2
	v_lshlrev_b32_e32 v2, 6, v2
	s_lshr_b32 s0, s0, 1
	s_mov_b32 s18, s85
	s_mov_b32 s26, s95
	v_and_b32_e32 v72, 28, v3
	v_and_b32_e32 v2, 0x80, v2
	s_and_b32 s0, s0, 0x60
	v_and_b32_e32 v3, 4, v3
	s_mov_b32 s25, 15
	s_movk_i32 s56, 0x1817
	s_ashr_i32 s11, s10, 31
	v_or3_b32 v67, v3, v2, s0
	v_mov_b32_e32 v71, v69
	v_or_b32_e32 v73, s0, v2
	s_mov_b32 s27, s26
	s_cmp_ge_u32 s95, 128
	s_cselect_b32 s100, 1, 0
	s_mov_b32 s101, 0
	s_cmp_eq_u32 s100, 0
	s_cbranch_scc0 .LBB0_302
	s_branch .LBB0_177

.LBB0_177:
	s_cmp_gt_i32 s27, s56
	s_mov_b64 s[0:1], -1
	s_cbranch_scc1 .LBB0_176
	s_cmpk_gt_i32 s27, 0xfff
	s_mov_b64 s[16:17], -1
	s_cbranch_scc0 .LBB0_187
	s_cmpk_gt_u32 s27, 0x17ff
	s_cbranch_scc0 .LBB0_184
	s_add_i32 s14, s27, 0xffffe800
	s_and_b32 s16, s27, 7
	s_cmp_gt_u32 s14, 15
	s_mov_b64 s[12:13], -1
	s_cbranch_scc0 .LBB0_182
	v_mov_b32_e32 v2, 0x23f98
	s_mov_b64 s[12:13], 0
	v_add_u32_e32 v2, 0, v2
	ds_read_b64 v[2:3], v2
	s_waitcnt lgkmcnt(0)
	v_readfirstlane_b32 s0, v2
	v_readfirstlane_b32 s1, v3
	s_add_u32 s0, s0, s22
	s_addc_u32 s1, s1, 0
	s_lshr_b32 s28, s16, 2
	s_and_b32 s31, s27, 3

.LBB0_238:
	s_cmp_eq_u32 s101, 2
	s_cbranch_scc1 .Lp8_done
	s_mul_i32 s0, s18, 24
	s_add_i32 s25, s26, s0
	s_mov_b32 s26, 8
	s_branch .LBB0_241

.LBB0_430:
	s_movk_i32 s34, 0x1000
	s_barrier
	s_cmp_eq_u32 s100, 1
	s_cbranch_scc0 .LBB0_431
	s_mov_b32 s101, 1
	s_lshl_b32 s22, s36, 20
	s_lshl_b32 s23, s36, 28
	s_waitcnt vmcnt(3)
	v_mov_b32_e32 v2, v0
	s_mov_b64 s[0:1], s[42:43]
	s_add_u32 s19, s0, 0x10a4c000
	s_addc_u32 s20, s1, 0
	s_add_u32 s2, s0, 0x14a4c000
	s_addc_u32 s3, s1, 0
	s_add_u32 s4, s0, 0x894c000
	s_addc_u32 s5, s1, 0
	v_readfirstlane_b32 s10, v2
	s_add_u32 s21, s0, 0x94c000
	s_addc_u32 s24, s1, 0
	v_lshlrev_b32_e32 v3, 1, v2
	s_ashr_i32 s0, s10, 1
	v_and_b32_e32 v70, 0x70, v3
	s_and_b32 s10, s0, 0xffffffe0
	v_lshlrev_b32_e32 v3, 2, v2
	v_lshlrev_b32_e32 v2, 6, v2
	s_lshr_b32 s0, s0, 1
	s_mov_b32 s18, s85
	s_mov_b32 s26, s95
	v_and_b32_e32 v72, 28, v3
	v_and_b32_e32 v2, 0x80, v2
	s_and_b32 s0, s0, 0x60
	v_and_b32_e32 v3, 4, v3
	s_mov_b32 s25, 15
	s_movk_i32 s56, 0x1817
	s_ashr_i32 s11, s10, 31
	v_or3_b32 v67, v3, v2, s0
	v_mov_b32_e32 v71, v69
	v_or_b32_e32 v73, s0, v2
	s_mov_b32 s27, s26
	s_branch .LBB0_177

.LBB0_961:
	s_mov_b32 s24, s66
	s_barrier
	s_branch .LBB0_962
.Lp8_conv:
	s_mov_b32 s57, s24
	s_mov_b32 s101, 2
	v_readlane_b32 s22, v247, 34
	s_waitcnt vmcnt(3)
	v_mov_b32_e32 v2, v0
	s_mov_b64 s[0:1], s[42:43]
	s_add_u32 s19, s0, 0x10a4c000
	s_addc_u32 s20, s1, 0
	s_add_u32 s2, s0, 0x14a4c000
	s_addc_u32 s3, s1, 0
	s_add_u32 s4, s0, 0x894c000
	s_addc_u32 s5, s1, 0
	v_readfirstlane_b32 s10, v2
	s_add_u32 s21, s0, 0x94c000
	s_addc_u32 s24, s1, 0
	v_lshlrev_b32_e32 v3, 1, v2
	s_ashr_i32 s0, s10, 1
	v_and_b32_e32 v70, 0x70, v3
	s_and_b32 s10, s0, 0xffffffe0
	v_lshlrev_b32_e32 v3, 2, v2
	v_lshlrev_b32_e32 v2, 6, v2
	s_lshr_b32 s0, s0, 1
	s_sub_i32 s18, s85, s96
	s_and_b32 s23, s22, 0x10000000
	s_and_b32 s22, s22, 0x100000
	s_mov_b32 s26, s95
	v_and_b32_e32 v72, 28, v3
	v_and_b32_e32 v2, 0x80, v2
	s_and_b32 s0, s0, 0x60
	v_and_b32_e32 v3, 4, v3
	s_mov_b32 s25, 100
	s_ashr_i32 s11, s10, 31
	v_or3_b32 v67, v3, v2, s0
	v_mov_b32_e32 v71, v69
	v_or_b32_e32 v73, s0, v2
	s_sub_i32 s27, s26, s96
	s_addk_i32 s27, 0xf00
	s_movk_i32 s56, 0x13ff
	s_branch .LBB0_177
.Lp8_done:
	s_mov_b32 s24, s57
	s_mov_b32 s101, 0
